# baseline (speedup 1.0000x reference)
.LBB1_80:
	s_or_b64 exec, exec, s[24:25]
	v_mad_u32_u24 v115, v233, s53, v226
	s_waitcnt lgkmcnt(0)
	s_barrier
	ds_read_b128 v[134:137], v115
	ds_read_b128 v[138:141], v115 offset:64
	s_waitcnt lgkmcnt(1)
	v_mfma_f32_16x16x32_bf16 v[116:119], v[46:49], v[134:137], v[118:121]
	v_add_u32_e32 v166, v191, v229
	v_mov_b32_e32 v167, v114
	s_mov_b32 s46, 0
	v_mfma_f32_16x16x32_bf16 v[120:123], v[74:77], v[134:137], v[122:125]
	v_mfma_f32_16x16x32_bf16 v[126:129], v[18:21], v[134:137], v[126:129]
	s_waitcnt lgkmcnt(0)
	v_mfma_f32_16x16x32_bf16 v[116:119], v[50:53], v[138:141], v[116:119]
	v_mfma_f32_16x16x32_bf16 v[120:123], v[78:81], v[138:141], v[120:123]
	v_mfma_f32_16x16x32_bf16 v[126:129], v[22:25], v[138:141], v[126:129]
	s_and_b64 s[70:71], exec, s[6:7]
	s_cbranch_scc1 .Lred_skip_0
	v_add_f32_dpp v246, v246, v246 quad_perm:[1,0,3,2] row_mask:0xf bank_mask:0xf bound_ctrl:1
	v_add_f32_dpp v247, v247, v247 quad_perm:[1,0,3,2] row_mask:0xf bank_mask:0xf bound_ctrl:1
	s_nop 0
	v_add_f32_dpp v246, v246, v246 quad_perm:[2,3,0,1] row_mask:0xf bank_mask:0xf bound_ctrl:1
	v_add_f32_dpp v247, v247, v247 quad_perm:[2,3,0,1] row_mask:0xf bank_mask:0xf bound_ctrl:1
	s_nop 0
	v_add_f32_dpp v246, v246, v246 row_half_mirror row_mask:0xf bank_mask:0xf bound_ctrl:1
	v_add_f32_dpp v247, v247, v247 row_half_mirror row_mask:0xf bank_mask:0xf bound_ctrl:1
	s_nop 0
	v_add_f32_dpp v246, v246, v246 row_mirror row_mask:0xf bank_mask:0xf bound_ctrl:1
	v_add_f32_dpp v247, v247, v247 row_mirror row_mask:0xf bank_mask:0xf bound_ctrl:1
	s_nop 0
	v_add_f32_dpp v246, v246, v246 row_bcast:15 row_mask:0x2 bank_mask:0xf
	v_add_f32_dpp v247, v247, v247 row_bcast:15 row_mask:0x2 bank_mask:0xf
	s_nop 0
	v_add_f32_dpp v246, v246, v246 row_bcast:15 row_mask:0x4 bank_mask:0xf
	v_add_f32_dpp v247, v247, v247 row_bcast:15 row_mask:0x4 bank_mask:0xf
	s_nop 0
	v_add_f32_dpp v246, v246, v246 row_bcast:15 row_mask:0x8 bank_mask:0xf
	v_add_f32_dpp v247, v247, v247 row_bcast:15 row_mask:0x8 bank_mask:0xf
	s_nop 0
	s_mov_b32 s62, 0
	s_mov_b32 s63, 0x10000
	s_and_saveexec_b64 s[70:71], s[62:63]
	ds_write_b64 v231, v[246:247]
	s_or_b64 exec, exec, s[70:71]

.LBB1_116:
	s_or_b64 exec, exec, s[24:25]
	v_mad_u32_u24 v115, v167, s53, v226
	s_waitcnt lgkmcnt(0)
	s_barrier
	ds_read_b128 v[134:137], v115
	ds_read_b128 v[138:141], v115 offset:64
	s_waitcnt lgkmcnt(1)
	v_mfma_f32_16x16x32_bf16 v[116:119], v[46:49], v[134:137], v[118:121]
	s_mov_b32 s46, 0
	v_or_b32_e32 v236, 32, v233
	v_mfma_f32_16x16x32_bf16 v[120:123], v[74:77], v[134:137], v[122:125]
	v_mfma_f32_16x16x32_bf16 v[126:129], v[18:21], v[134:137], v[126:129]
	s_waitcnt lgkmcnt(0)
	v_mfma_f32_16x16x32_bf16 v[116:119], v[50:53], v[138:141], v[116:119]
	v_mfma_f32_16x16x32_bf16 v[120:123], v[78:81], v[138:141], v[120:123]
	v_mfma_f32_16x16x32_bf16 v[126:129], v[22:25], v[138:141], v[126:129]
	s_and_b64 s[70:71], exec, s[6:7]
	s_cbranch_scc1 .Lred_skip_1
	v_add_f32_dpp v246, v246, v246 quad_perm:[1,0,3,2] row_mask:0xf bank_mask:0xf bound_ctrl:1
	v_add_f32_dpp v247, v247, v247 quad_perm:[1,0,3,2] row_mask:0xf bank_mask:0xf bound_ctrl:1
	s_nop 0
	v_add_f32_dpp v246, v246, v246 quad_perm:[2,3,0,1] row_mask:0xf bank_mask:0xf bound_ctrl:1
	v_add_f32_dpp v247, v247, v247 quad_perm:[2,3,0,1] row_mask:0xf bank_mask:0xf bound_ctrl:1
	s_nop 0
	v_add_f32_dpp v246, v246, v246 row_half_mirror row_mask:0xf bank_mask:0xf bound_ctrl:1
	v_add_f32_dpp v247, v247, v247 row_half_mirror row_mask:0xf bank_mask:0xf bound_ctrl:1
	s_nop 0
	v_add_f32_dpp v246, v246, v246 row_mirror row_mask:0xf bank_mask:0xf bound_ctrl:1
	v_add_f32_dpp v247, v247, v247 row_mirror row_mask:0xf bank_mask:0xf bound_ctrl:1
	s_nop 0
	v_add_f32_dpp v246, v246, v246 row_bcast:15 row_mask:0x2 bank_mask:0xf
	v_add_f32_dpp v247, v247, v247 row_bcast:15 row_mask:0x2 bank_mask:0xf
	s_nop 0
	v_add_f32_dpp v246, v246, v246 row_bcast:15 row_mask:0x4 bank_mask:0xf
	v_add_f32_dpp v247, v247, v247 row_bcast:15 row_mask:0x4 bank_mask:0xf
	s_nop 0
	v_add_f32_dpp v246, v246, v246 row_bcast:15 row_mask:0x8 bank_mask:0xf
	v_add_f32_dpp v247, v247, v247 row_bcast:15 row_mask:0x8 bank_mask:0xf
	s_nop 0
	s_mov_b32 s62, 0
	s_mov_b32 s63, 0x10000
	s_and_saveexec_b64 s[70:71], s[62:63]
	ds_write_b64 v231, v[246:247] offset:24
	s_or_b64 exec, exec, s[70:71]

.LBB1_152:
	s_or_b64 exec, exec, s[24:25]
	v_mad_u32_u24 v115, v236, s53, v226
	s_waitcnt lgkmcnt(0)
	s_barrier
	ds_read_b128 v[134:137], v115
	ds_read_b128 v[138:141], v115 offset:64
	s_waitcnt lgkmcnt(1)
	v_mfma_f32_16x16x32_bf16 v[116:119], v[46:49], v[134:137], v[118:121]
	s_mov_b32 s48, 0
	s_cmpk_lg_i32 s40, 0x1810
	v_or_b32_e32 v167, 48, v233
	v_mfma_f32_16x16x32_bf16 v[120:123], v[74:77], v[134:137], v[122:125]
	s_cselect_b64 s[24:25], -1, 0
	v_mfma_f32_16x16x32_bf16 v[126:129], v[18:21], v[134:137], v[126:129]
	s_waitcnt lgkmcnt(0)
	v_mfma_f32_16x16x32_bf16 v[116:119], v[50:53], v[138:141], v[116:119]
	v_mfma_f32_16x16x32_bf16 v[120:123], v[78:81], v[138:141], v[120:123]
	v_mfma_f32_16x16x32_bf16 v[126:129], v[22:25], v[138:141], v[126:129]
	s_and_b64 s[70:71], exec, s[6:7]
	s_cbranch_scc1 .Lred_skip_2
	v_add_f32_dpp v246, v246, v246 quad_perm:[1,0,3,2] row_mask:0xf bank_mask:0xf bound_ctrl:1
	v_add_f32_dpp v247, v247, v247 quad_perm:[1,0,3,2] row_mask:0xf bank_mask:0xf bound_ctrl:1
	s_nop 0
	v_add_f32_dpp v246, v246, v246 quad_perm:[2,3,0,1] row_mask:0xf bank_mask:0xf bound_ctrl:1
	v_add_f32_dpp v247, v247, v247 quad_perm:[2,3,0,1] row_mask:0xf bank_mask:0xf bound_ctrl:1
	s_nop 0
	v_add_f32_dpp v246, v246, v246 row_half_mirror row_mask:0xf bank_mask:0xf bound_ctrl:1
	v_add_f32_dpp v247, v247, v247 row_half_mirror row_mask:0xf bank_mask:0xf bound_ctrl:1
	s_nop 0
	v_add_f32_dpp v246, v246, v246 row_mirror row_mask:0xf bank_mask:0xf bound_ctrl:1
	v_add_f32_dpp v247, v247, v247 row_mirror row_mask:0xf bank_mask:0xf bound_ctrl:1
	s_nop 0
	v_add_f32_dpp v246, v246, v246 row_bcast:15 row_mask:0x2 bank_mask:0xf
	v_add_f32_dpp v247, v247, v247 row_bcast:15 row_mask:0x2 bank_mask:0xf
	s_nop 0
	v_add_f32_dpp v246, v246, v246 row_bcast:15 row_mask:0x4 bank_mask:0xf
	v_add_f32_dpp v247, v247, v247 row_bcast:15 row_mask:0x4 bank_mask:0xf
	s_nop 0
	v_add_f32_dpp v246, v246, v246 row_bcast:15 row_mask:0x8 bank_mask:0xf
	v_add_f32_dpp v247, v247, v247 row_bcast:15 row_mask:0x8 bank_mask:0xf
	s_nop 0
	s_mov_b32 s62, 0
	s_mov_b32 s63, 0x10000
	s_and_saveexec_b64 s[70:71], s[62:63]
	ds_write_b64 v231, v[246:247] offset:48
	s_or_b64 exec, exec, s[70:71]

.LBB1_192:
	s_or_b64 exec, exec, s[42:43]
	v_mad_u32_u24 v115, v167, s53, v226
	s_waitcnt lgkmcnt(0)
	s_barrier
	ds_read_b128 v[134:137], v115
	ds_read_b128 v[138:141], v115 offset:64
	s_waitcnt lgkmcnt(1)
	v_mfma_f32_16x16x32_bf16 v[116:119], v[18:21], v[134:137], v[118:121]
	s_and_b64 vcc, exec, s[24:25]
	v_mfma_f32_16x16x32_bf16 v[120:123], v[46:49], v[134:137], v[122:125]
	v_mfma_f32_16x16x32_bf16 v[124:127], v[74:77], v[134:137], v[126:129]
	s_waitcnt lgkmcnt(0)
	v_mfma_f32_16x16x32_bf16 v[116:119], v[22:25], v[138:141], v[116:119]
	v_mfma_f32_16x16x32_bf16 v[124:127], v[78:81], v[138:141], v[124:127]
	v_mfma_f32_16x16x32_bf16 v[120:123], v[50:53], v[138:141], v[120:123]
	s_and_b64 s[70:71], exec, s[6:7]
	s_cbranch_scc1 .Lred_skip_3
	v_add_f32_dpp v246, v246, v246 quad_perm:[1,0,3,2] row_mask:0xf bank_mask:0xf bound_ctrl:1
	v_add_f32_dpp v247, v247, v247 quad_perm:[1,0,3,2] row_mask:0xf bank_mask:0xf bound_ctrl:1
	s_nop 0
	v_add_f32_dpp v246, v246, v246 quad_perm:[2,3,0,1] row_mask:0xf bank_mask:0xf bound_ctrl:1
	v_add_f32_dpp v247, v247, v247 quad_perm:[2,3,0,1] row_mask:0xf bank_mask:0xf bound_ctrl:1
	s_nop 0
	v_add_f32_dpp v246, v246, v246 row_half_mirror row_mask:0xf bank_mask:0xf bound_ctrl:1
	v_add_f32_dpp v247, v247, v247 row_half_mirror row_mask:0xf bank_mask:0xf bound_ctrl:1
	s_nop 0
	v_add_f32_dpp v246, v246, v246 row_mirror row_mask:0xf bank_mask:0xf bound_ctrl:1
	v_add_f32_dpp v247, v247, v247 row_mirror row_mask:0xf bank_mask:0xf bound_ctrl:1
	s_nop 0
	v_add_f32_dpp v246, v246, v246 row_bcast:15 row_mask:0x2 bank_mask:0xf
	v_add_f32_dpp v247, v247, v247 row_bcast:15 row_mask:0x2 bank_mask:0xf
	s_nop 0
	v_add_f32_dpp v246, v246, v246 row_bcast:15 row_mask:0x4 bank_mask:0xf
	v_add_f32_dpp v247, v247, v247 row_bcast:15 row_mask:0x4 bank_mask:0xf
	s_nop 0
	v_add_f32_dpp v246, v246, v246 row_bcast:15 row_mask:0x8 bank_mask:0xf
	v_add_f32_dpp v247, v247, v247 row_bcast:15 row_mask:0x8 bank_mask:0xf
	s_nop 0
	s_mov_b32 s62, 0
	s_mov_b32 s63, 0x10000
	s_and_saveexec_b64 s[70:71], s[62:63]
	ds_write_b64 v231, v[246:247] offset:72
	s_or_b64 exec, exec, s[70:71]
